# balanced pairing flipped: heavy chunk of each SIMD pair goes to the older wave (0-3), light to 4-7
# baseline (speedup 1.0000x reference)
.LBB1_141:
	s_or_b64 exec, exec, s[6:7]
	v_and_b32_e32 v1, 31, v0
	s_waitcnt lgkmcnt(0)
	v_lshlrev_b32_e32 v2, 2, v1
	v_or_b32_e32 v22, 32, v8
	s_barrier
	v_readfirstlane_b32 s95, v9
	v_min_u32_e32 v24, 8, v1
	v_mov_b32_e32 v25, 0x12810
	v_lshl_add_u32 v25, v24, 10, v25
	ds_read_b32 v25, v25
	v_mov_b32_e32 v27, 0
	s_waitcnt lgkmcnt(0)
	v_mov_b32_e32 v26, v25
	s_nop 1
	v_mov_b32_dpp v26, v25 row_shl:1 row_mask:0xf bank_mask:0xf
	v_sub_u32_e32 v26, v26, v25
	v_lshl_or_b32 v26, v26, 3, v24
	s_nop 1
	v_readlane_b32 s86, v26, 0
	v_readlane_b32 s87, v26, 1
	v_readlane_b32 s88, v26, 2
	v_readlane_b32 s89, v26, 3
	v_readlane_b32 s90, v26, 4
	v_readlane_b32 s91, v26, 5
	v_readlane_b32 s92, v26, 6
	v_readlane_b32 s93, v26, 7
	v_cmp_lt_u32_e32 vcc, s86, v26
	v_addc_co_u32_e32 v27, vcc, 0, v27, vcc
	v_cmp_lt_u32_e32 vcc, s87, v26
	v_addc_co_u32_e32 v27, vcc, 0, v27, vcc
	v_cmp_lt_u32_e32 vcc, s88, v26
	v_addc_co_u32_e32 v27, vcc, 0, v27, vcc
	v_cmp_lt_u32_e32 vcc, s89, v26
	v_addc_co_u32_e32 v27, vcc, 0, v27, vcc
	v_cmp_lt_u32_e32 vcc, s90, v26
	v_addc_co_u32_e32 v27, vcc, 0, v27, vcc
	v_cmp_lt_u32_e32 vcc, s91, v26
	v_addc_co_u32_e32 v27, vcc, 0, v27, vcc
	v_cmp_lt_u32_e32 vcc, s92, v26
	v_addc_co_u32_e32 v27, vcc, 0, v27, vcc
	v_cmp_lt_u32_e32 vcc, s93, v26
	v_addc_co_u32_e32 v27, vcc, 0, v27, vcc
	v_sub_u32_e32 v24, 7, v27
	v_add_u32_e32 v25, 4, v27
	v_cmp_gt_u32_e32 vcc, 4, v27
	v_cndmask_b32_e32 v27, v24, v25, vcc
	s_nop 0
	v_cmp_eq_u32_e32 vcc, s95, v27
	s_ff1_i32_b64 s95, vcc
	v_mov_b32_e32 v9, s95
	s_lshl_b32 s84, s95, 3
	s_add_u32 s85, s84, 8
	v_lshlrev_b32_e32 v3, 2, v22
	s_waitcnt vmcnt(0)
	v_mov_b32_e32 v18, v108
	v_mov_b32_e32 v19, v109
	v_mov_b32_e32 v20, v110
	v_mov_b32_e32 v16, v111
	v_mov_b32_e32 v17, v112
	v_mov_b32_e32 v12, v113
	v_mov_b32_e32 v13, v114
	v_mov_b32_e32 v15, v115
	v_mov_b32_e32 v4, 0x180
	v_lshl_or_b32 v23, v8, 2, v4
	v_mov_b32_e32 v21, v116
	v_mov_b32_e32 v4, v117
	v_mov_b32_e32 v5, v118
	v_mov_b32_e32 v10, v119
	v_mov_b32_e32 v3, 0x12810
	v_lshl_add_u32 v23, v9, 10, v3
	ds_read2_b32 v[24:25], v23 offset1:32
	v_add_u32_e32 v2, v23, v2
	ds_read2_b32 v[230:231], v2 offset1:1
	v_lshlrev_b32_e32 v26, 8, v9
	s_lshl_b32 s2, s2, 11
	v_or3_b32 v235, v26, s2, v1
	s_mov_b32 s12, 0x7a120
	s_waitcnt lgkmcnt(1)
	v_readfirstlane_b32 s13, v24
	v_readfirstlane_b32 s6, v25
	v_cmp_gt_i32_e32 vcc, s12, v235
	v_mov_b32_e32 v2, 0
	v_mov_b32_e32 v238, 0
	s_and_saveexec_b64 s[2:3], vcc
	s_cbranch_execz .LBB1_143
	v_ashrrev_i32_e32 v25, 31, v235
	v_mov_b32_e32 v24, v235
	v_lshl_add_u64 v[24:25], v[24:25], 2, s[50:51]
	global_load_dword v238, v[24:25], off
